# grid barrier: waiting workgroups poll the global generation word directly instead of their XCD's word (one poll round trip less after the last arrival); per-XCD generation update dropped
# speedup vs baseline: 1.0121x; 1.0121x over previous
.LBB0_296:
	s_or_b64 exec, exec, s[6:7]
	v_cvt_f32_u32_e32 v6, v4
	s_waitcnt vmcnt(0)
	v_readfirstlane_b32 s4, v5
	v_sub_u32_e32 v5, 0, v4
	v_rcp_iflag_f32_e32 v6, v6
	v_add_u32_e32 v7, s4, v3
	v_mul_f32_e32 v6, 0x4f7ffffe, v6
	v_cvt_u32_f32_e32 v6, v6
	v_mul_lo_u32 v3, v5, v6
	v_mul_hi_u32 v3, v6, v3
	v_add_u32_e32 v3, v6, v3
	v_mul_hi_u32 v3, v7, v3
	v_mul_lo_u32 v5, v3, v4
	v_sub_u32_e32 v5, v7, v5
	v_add_u32_e32 v6, 1, v3
	v_cmp_ge_u32_e32 vcc, v5, v4
	s_nop 1
	v_cndmask_b32_e32 v3, v3, v6, vcc
	v_sub_u32_e32 v6, v5, v4
	v_cndmask_b32_e32 v5, v5, v6, vcc
	v_add_u32_e32 v6, 1, v3
	v_cmp_ge_u32_e32 vcc, v5, v4
	v_add_u32_e32 v5, 1, v7
	s_nop 0
	v_cndmask_b32_e32 v3, v3, v6, vcc
	v_mul_lo_u32 v6, v4, v3
	v_add_u32_e32 v4, v6, v4
	v_cmp_ne_u32_e32 vcc, v5, v4
	s_and_saveexec_b64 s[4:5], vcc
	s_xor_b64 s[4:5], exec, s[4:5]
	s_cbranch_execz .LBB0_310
	s_waitcnt lgkmcnt(0)
	v_mov_b32_e32 v2, 0x7100
	global_load_dword v2, v2, s[56:57] offset:1024 sc1
	s_add_u32 s14, s56, 0x7500
	s_addc_u32 s15, s57, 0
	s_waitcnt vmcnt(0)
	v_cmp_eq_u32_e32 vcc, v2, v3
	s_and_saveexec_b64 s[6:7], vcc
	s_cbranch_execz .LBB0_309
	s_add_u32 s8, s56, 0x4200
	s_addc_u32 s9, s57, 0
	s_mov_b32 s10, 1
	s_mov_b64 s[24:25], 0
	v_mov_b32_e32 v2, 0
	s_branch .LBB0_300

.LBB0_327:
	s_or_b64 exec, exec, s[4:5]
	s_mov_b64 s[4:5], exec
	v_mbcnt_lo_u32_b32 v2, s4, 0
	v_mbcnt_hi_u32_b32 v2, s5, v2
	v_cmp_eq_u32_e32 vcc, 0, v2
	s_waitcnt vmcnt(0)
	buffer_inv sc1
	s_and_saveexec_b64 s[6:7], vcc
	s_cbranch_execz .LBB0_329
	s_bcnt1_i32_b64 s4, s[4:5]
	v_mov_b32_e32 v2, 0x2000
	v_mov_b32_e32 v3, s4
	s_nop 0

.LBB0_484:
	s_or_b64 exec, exec, s[6:7]
	v_cvt_f32_u32_e32 v6, v4
	s_waitcnt vmcnt(0)
	v_readfirstlane_b32 s4, v5
	v_sub_u32_e32 v5, 0, v4
	v_rcp_iflag_f32_e32 v6, v6
	v_add_u32_e32 v7, s4, v3
	v_mul_f32_e32 v6, 0x4f7ffffe, v6
	v_cvt_u32_f32_e32 v6, v6
	v_mul_lo_u32 v3, v5, v6
	v_mul_hi_u32 v3, v6, v3
	v_add_u32_e32 v3, v6, v3
	v_mul_hi_u32 v3, v7, v3
	v_mul_lo_u32 v5, v3, v4
	v_sub_u32_e32 v5, v7, v5
	v_add_u32_e32 v6, 1, v3
	v_cmp_ge_u32_e32 vcc, v5, v4
	s_nop 1
	v_cndmask_b32_e32 v3, v3, v6, vcc
	v_sub_u32_e32 v6, v5, v4
	v_cndmask_b32_e32 v5, v5, v6, vcc
	v_add_u32_e32 v6, 1, v3
	v_cmp_ge_u32_e32 vcc, v5, v4
	v_add_u32_e32 v5, 1, v7
	s_nop 0
	v_cndmask_b32_e32 v3, v3, v6, vcc
	v_mul_lo_u32 v6, v4, v3
	v_add_u32_e32 v4, v6, v4
	v_cmp_ne_u32_e32 vcc, v5, v4
	s_and_saveexec_b64 s[4:5], vcc
	s_xor_b64 s[4:5], exec, s[4:5]
	s_cbranch_execz .LBB0_498
	s_waitcnt lgkmcnt(0)
	v_mov_b32_e32 v2, 0x7100
	global_load_dword v2, v2, s[56:57] offset:1024 sc1
	s_add_u32 s14, s56, 0x7500
	s_addc_u32 s15, s57, 0
	s_waitcnt vmcnt(0)
	v_cmp_eq_u32_e32 vcc, v2, v3
	s_and_saveexec_b64 s[6:7], vcc
	s_cbranch_execz .LBB0_497
	s_add_u32 s8, s56, 0x4200
	s_addc_u32 s9, s57, 0
	s_mov_b32 s10, 1
	s_mov_b64 s[36:37], 0
	v_mov_b32_e32 v2, 0
	s_branch .LBB0_488

.LBB0_566:
	s_or_b64 exec, exec, s[6:7]
	v_cvt_f32_u32_e32 v6, v4
	s_waitcnt vmcnt(0)
	v_readfirstlane_b32 s4, v5
	v_sub_u32_e32 v5, 0, v4
	v_rcp_iflag_f32_e32 v6, v6
	v_add_u32_e32 v7, s4, v3
	v_mul_f32_e32 v6, 0x4f7ffffe, v6
	v_cvt_u32_f32_e32 v6, v6
	v_mul_lo_u32 v3, v5, v6
	v_mul_hi_u32 v3, v6, v3
	v_add_u32_e32 v3, v6, v3
	v_mul_hi_u32 v3, v7, v3
	v_mul_lo_u32 v5, v3, v4
	v_sub_u32_e32 v5, v7, v5
	v_add_u32_e32 v6, 1, v3
	v_cmp_ge_u32_e32 vcc, v5, v4
	s_nop 1
	v_cndmask_b32_e32 v3, v3, v6, vcc
	v_sub_u32_e32 v6, v5, v4
	v_cndmask_b32_e32 v5, v5, v6, vcc
	v_add_u32_e32 v6, 1, v3
	v_cmp_ge_u32_e32 vcc, v5, v4
	v_add_u32_e32 v5, 1, v7
	s_nop 0
	v_cndmask_b32_e32 v3, v3, v6, vcc
	v_mul_lo_u32 v6, v4, v3
	v_add_u32_e32 v4, v6, v4
	v_cmp_ne_u32_e32 vcc, v5, v4
	s_and_saveexec_b64 s[4:5], vcc
	s_xor_b64 s[4:5], exec, s[4:5]
	s_cbranch_execz .LBB0_580
	s_waitcnt lgkmcnt(0)
	v_mov_b32_e32 v2, 0x7100
	global_load_dword v2, v2, s[56:57] offset:1024 sc1
	s_add_u32 s14, s56, 0x7500
	s_addc_u32 s15, s57, 0
	s_waitcnt vmcnt(0)
	v_cmp_eq_u32_e32 vcc, v2, v3
	s_and_saveexec_b64 s[6:7], vcc
	s_cbranch_execz .LBB0_579
	s_add_u32 s8, s56, 0x4200
	s_addc_u32 s9, s57, 0
	s_mov_b32 s10, 1
	s_mov_b64 s[40:41], 0
	v_mov_b32_e32 v2, 0
	s_branch .LBB0_570

.LBB0_649:
	s_or_b64 exec, exec, s[6:7]
	v_cvt_f32_u32_e32 v6, v4
	s_waitcnt vmcnt(0)
	v_readfirstlane_b32 s4, v5
	v_sub_u32_e32 v5, 0, v4
	v_rcp_iflag_f32_e32 v6, v6
	v_add_u32_e32 v7, s4, v3
	v_mul_f32_e32 v6, 0x4f7ffffe, v6
	v_cvt_u32_f32_e32 v6, v6
	v_mul_lo_u32 v3, v5, v6
	v_mul_hi_u32 v3, v6, v3
	v_add_u32_e32 v3, v6, v3
	v_mul_hi_u32 v3, v7, v3
	v_mul_lo_u32 v5, v3, v4
	v_sub_u32_e32 v5, v7, v5
	v_add_u32_e32 v6, 1, v3
	v_cmp_ge_u32_e32 vcc, v5, v4
	s_nop 1
	v_cndmask_b32_e32 v3, v3, v6, vcc
	v_sub_u32_e32 v6, v5, v4
	v_cndmask_b32_e32 v5, v5, v6, vcc
	v_add_u32_e32 v6, 1, v3
	v_cmp_ge_u32_e32 vcc, v5, v4
	v_add_u32_e32 v5, 1, v7
	s_nop 0
	v_cndmask_b32_e32 v3, v3, v6, vcc
	v_mul_lo_u32 v6, v4, v3
	v_add_u32_e32 v4, v6, v4
	v_cmp_ne_u32_e32 vcc, v5, v4
	s_and_saveexec_b64 s[4:5], vcc
	s_xor_b64 s[4:5], exec, s[4:5]
	s_cbranch_execz .LBB0_663
	s_waitcnt lgkmcnt(0)
	v_mov_b32_e32 v2, 0x7100
	global_load_dword v2, v2, s[56:57] offset:1024 sc1
	s_add_u32 s14, s56, 0x7500
	s_addc_u32 s15, s57, 0
	s_waitcnt vmcnt(0)
	v_cmp_eq_u32_e32 vcc, v2, v3
	s_and_saveexec_b64 s[6:7], vcc
	s_cbranch_execz .LBB0_662
	s_add_u32 s8, s56, 0x4200
	s_addc_u32 s9, s57, 0
	s_mov_b32 s10, 1
	s_mov_b64 s[22:23], 0
	v_mov_b32_e32 v2, 0
	s_branch .LBB0_653

.LBB0_804:
	s_or_b64 exec, exec, s[6:7]
	v_cvt_f32_u32_e32 v6, v4
	s_waitcnt vmcnt(0)
	v_readfirstlane_b32 s4, v5
	v_sub_u32_e32 v5, 0, v4
	v_rcp_iflag_f32_e32 v6, v6
	v_add_u32_e32 v7, s4, v3
	v_mul_f32_e32 v6, 0x4f7ffffe, v6
	v_cvt_u32_f32_e32 v6, v6
	v_mul_lo_u32 v3, v5, v6
	v_mul_hi_u32 v3, v6, v3
	v_add_u32_e32 v3, v6, v3
	v_mul_hi_u32 v3, v7, v3
	v_mul_lo_u32 v5, v3, v4
	v_sub_u32_e32 v5, v7, v5
	v_add_u32_e32 v6, 1, v3
	v_cmp_ge_u32_e32 vcc, v5, v4
	s_nop 1
	v_cndmask_b32_e32 v3, v3, v6, vcc
	v_sub_u32_e32 v6, v5, v4
	v_cndmask_b32_e32 v5, v5, v6, vcc
	v_add_u32_e32 v6, 1, v3
	v_cmp_ge_u32_e32 vcc, v5, v4
	v_add_u32_e32 v5, 1, v7
	s_nop 0
	v_cndmask_b32_e32 v3, v3, v6, vcc
	v_mul_lo_u32 v6, v4, v3
	v_add_u32_e32 v4, v6, v4
	v_cmp_ne_u32_e32 vcc, v5, v4
	s_and_saveexec_b64 s[4:5], vcc
	s_xor_b64 s[4:5], exec, s[4:5]
	s_cbranch_execz .LBB0_818
	s_waitcnt lgkmcnt(0)
	v_mov_b32_e32 v2, 0x7100
	global_load_dword v2, v2, s[56:57] offset:1024 sc1
	s_add_u32 s14, s56, 0x7500
	s_addc_u32 s15, s57, 0
	s_waitcnt vmcnt(0)
	v_cmp_eq_u32_e32 vcc, v2, v3
	s_and_saveexec_b64 s[6:7], vcc
	s_cbranch_execz .LBB0_817
	s_add_u32 s8, s56, 0x4200
	s_addc_u32 s9, s57, 0
	s_mov_b32 s10, 1
	s_mov_b64 s[16:17], 0
	v_mov_b32_e32 v2, 0
	s_branch .LBB0_808

.LBB0_886:
	s_or_b64 exec, exec, s[6:7]
	v_cvt_f32_u32_e32 v6, v4
	s_waitcnt vmcnt(0)
	v_readfirstlane_b32 s4, v5
	v_sub_u32_e32 v5, 0, v4
	v_rcp_iflag_f32_e32 v6, v6
	v_add_u32_e32 v7, s4, v3
	v_mul_f32_e32 v6, 0x4f7ffffe, v6
	v_cvt_u32_f32_e32 v6, v6
	v_mul_lo_u32 v3, v5, v6
	v_mul_hi_u32 v3, v6, v3
	v_add_u32_e32 v3, v6, v3
	v_mul_hi_u32 v3, v7, v3
	v_mul_lo_u32 v5, v3, v4
	v_sub_u32_e32 v5, v7, v5
	v_add_u32_e32 v6, 1, v3
	v_cmp_ge_u32_e32 vcc, v5, v4
	s_nop 1
	v_cndmask_b32_e32 v3, v3, v6, vcc
	v_sub_u32_e32 v6, v5, v4
	v_cndmask_b32_e32 v5, v5, v6, vcc
	v_add_u32_e32 v6, 1, v3
	v_cmp_ge_u32_e32 vcc, v5, v4
	v_add_u32_e32 v5, 1, v7
	s_nop 0
	v_cndmask_b32_e32 v3, v3, v6, vcc
	v_mul_lo_u32 v6, v4, v3
	v_add_u32_e32 v4, v6, v4
	v_cmp_ne_u32_e32 vcc, v5, v4
	s_and_saveexec_b64 s[4:5], vcc
	s_xor_b64 s[4:5], exec, s[4:5]
	s_cbranch_execz .LBB0_900
	s_waitcnt lgkmcnt(0)
	v_mov_b32_e32 v2, 0x7100
	global_load_dword v2, v2, s[56:57] offset:1024 sc1
	s_add_u32 s14, s56, 0x7500
	s_addc_u32 s15, s57, 0
	s_waitcnt vmcnt(0)
	v_cmp_eq_u32_e32 vcc, v2, v3
	s_and_saveexec_b64 s[6:7], vcc
	s_cbranch_execz .LBB0_899
	s_add_u32 s8, s56, 0x4200
	s_addc_u32 s9, s57, 0
	s_mov_b32 s10, 1
	s_mov_b64 s[26:27], 0
	v_mov_b32_e32 v2, 0
	s_branch .LBB0_890

.LBB0_1251:
	s_or_b64 exec, exec, s[8:9]
	v_cvt_f32_u32_e32 v6, v4
	s_waitcnt vmcnt(0)
	v_readfirstlane_b32 s6, v5
	v_sub_u32_e32 v5, 0, v4
	v_rcp_iflag_f32_e32 v6, v6
	v_add_u32_e32 v7, s6, v3
	v_mul_f32_e32 v6, 0x4f7ffffe, v6
	v_cvt_u32_f32_e32 v6, v6
	v_mul_lo_u32 v3, v5, v6
	v_mul_hi_u32 v3, v6, v3
	v_add_u32_e32 v3, v6, v3
	v_mul_hi_u32 v3, v7, v3
	v_mul_lo_u32 v5, v3, v4
	v_sub_u32_e32 v5, v7, v5
	v_add_u32_e32 v6, 1, v3
	v_cmp_ge_u32_e32 vcc, v5, v4
	s_nop 1
	v_cndmask_b32_e32 v3, v3, v6, vcc
	v_sub_u32_e32 v6, v5, v4
	v_cndmask_b32_e32 v5, v5, v6, vcc
	v_add_u32_e32 v6, 1, v3
	v_cmp_ge_u32_e32 vcc, v5, v4
	v_add_u32_e32 v5, 1, v7
	s_nop 0
	v_cndmask_b32_e32 v3, v3, v6, vcc
	v_mul_lo_u32 v6, v4, v3
	v_add_u32_e32 v4, v6, v4
	v_cmp_ne_u32_e32 vcc, v5, v4
	s_and_saveexec_b64 s[6:7], vcc
	s_xor_b64 s[6:7], exec, s[6:7]
	s_cbranch_execz .LBB0_1265
	s_waitcnt lgkmcnt(0)
	v_mov_b32_e32 v2, 0x7100
	global_load_dword v2, v2, s[56:57] offset:1024 sc1
	s_add_u32 s16, s56, 0x7500
	s_addc_u32 s17, s57, 0
	s_waitcnt vmcnt(0)
	v_cmp_eq_u32_e32 vcc, v2, v3
	s_and_saveexec_b64 s[8:9], vcc
	s_cbranch_execz .LBB0_1264
	s_add_u32 s14, s56, 0x4200
	s_addc_u32 s15, s57, 0
	s_mov_b32 s10, 1
	s_mov_b64 s[18:19], 0
	v_mov_b32_e32 v2, 0
	s_branch .LBB0_1255

.LBB0_1282:
	s_or_b64 exec, exec, s[6:7]
	s_mov_b64 s[6:7], exec
	v_mbcnt_lo_u32_b32 v2, s6, 0
	v_mbcnt_hi_u32_b32 v2, s7, v2
	v_cmp_eq_u32_e32 vcc, 0, v2
	s_waitcnt vmcnt(0)
	buffer_inv sc1
	s_and_saveexec_b64 s[8:9], vcc
	s_cbranch_execz .LBB0_1284
	s_bcnt1_i32_b64 s6, s[6:7]
	v_mov_b32_e32 v2, 0x2000
	v_mov_b32_e32 v3, s6
	s_nop 0

.LBB0_1642:
	s_or_b64 exec, exec, s[6:7]
	v_cvt_f32_u32_e32 v6, v4
	s_waitcnt vmcnt(0)
	v_readfirstlane_b32 s4, v5
	v_sub_u32_e32 v5, 0, v4
	v_rcp_iflag_f32_e32 v6, v6
	v_add_u32_e32 v7, s4, v3
	v_mul_f32_e32 v6, 0x4f7ffffe, v6
	v_cvt_u32_f32_e32 v6, v6
	v_mul_lo_u32 v3, v5, v6
	v_mul_hi_u32 v3, v6, v3
	v_add_u32_e32 v3, v6, v3
	v_mul_hi_u32 v3, v7, v3
	v_mul_lo_u32 v5, v3, v4
	v_sub_u32_e32 v5, v7, v5
	v_add_u32_e32 v6, 1, v3
	v_cmp_ge_u32_e32 vcc, v5, v4
	s_nop 1
	v_cndmask_b32_e32 v3, v3, v6, vcc
	v_sub_u32_e32 v6, v5, v4
	v_cndmask_b32_e32 v5, v5, v6, vcc
	v_add_u32_e32 v6, 1, v3
	v_cmp_ge_u32_e32 vcc, v5, v4
	v_add_u32_e32 v5, 1, v7
	s_nop 0
	v_cndmask_b32_e32 v3, v3, v6, vcc
	v_mul_lo_u32 v6, v4, v3
	v_add_u32_e32 v4, v6, v4
	v_cmp_ne_u32_e32 vcc, v5, v4
	s_and_saveexec_b64 s[4:5], vcc
	s_xor_b64 s[4:5], exec, s[4:5]
	s_cbranch_execz .LBB0_1656
	s_waitcnt lgkmcnt(0)
	v_mov_b32_e32 v2, 0x7100
	global_load_dword v2, v2, s[56:57] offset:1024 sc1
	s_add_u32 s10, s56, 0x7500
	s_addc_u32 s11, s57, 0
	s_waitcnt vmcnt(0)
	v_cmp_eq_u32_e32 vcc, v2, v3
	s_and_saveexec_b64 s[6:7], vcc
	s_cbranch_execz .LBB0_1655
	s_add_u32 s8, s56, 0x4200
	s_addc_u32 s9, s57, 0
	s_mov_b32 s28, 1
	s_mov_b64 s[12:13], 0
	v_mov_b32_e32 v2, 0
	s_branch .LBB0_1646
